# RowExch: the acquire invalidate issued right after the flag add (before the poll) instead of after the poll, P4 and P7
# baseline (speedup 1.0000x reference)
;     __device__ __forceinline__ bool run(const f32x4 (&v)[2][2][4][2], const Unit& u, int wr, int wc, int fr, int fq, PG8_LAS unsigned char* lds, int wid, int lane) const {
;     ...
;         asm volatile("s_waitcnt lgkmcnt(0)" ::: "memory"); __builtin_amdgcn_s_barrier(); asm volatile("" ::: "memory");
;         const int row = wid * 32 + (lane & 31);
;         if (lane < 32) { const float t = (P[row * 4 + 0] + P[row * 4 + 1]) + (P[row * 4 + 2] + P[row * 4 + 3]);
;             __hip_atomic_store((unsigned*)xbuf + ((size_t)(pm * BM + row) * 4 + pn), __float_as_uint(t), __ATOMIC_RELAXED, __HIP_MEMORY_SCOPE_AGENT); }
;         asm volatile("s_waitcnt vmcnt(0)" ::: "memory");
;         if (lane == 0) __hip_atomic_fetch_add(cnt + 64 * pm, 1u, __ATOMIC_RELAXED, __HIP_MEMORY_SCOPE_AGENT);
.LBB0_684:
	s_or_b64 exec, exec, s[10:11]
	s_waitcnt vmcnt(0)
	s_add_u32 s17, s78, 0x20000
	s_addc_u32 s20, s79, 0
	v_cmp_ne_u32_e64 s[12:13], 0, v187
	v_cmp_eq_u32_e64 s[10:11], 0, v187
	s_and_saveexec_b64 s[4:5], s[10:11]
	s_cbranch_execz .LBB0_687
	s_mov_b64 s[14:15], exec
	v_mbcnt_lo_u32_b32 v1, s14, 0
	v_mbcnt_hi_u32_b32 v1, s15, v1
	v_cmp_eq_u32_e32 vcc, 0, v1
	s_and_b64 s[22:23], exec, vcc
	s_mov_b64 exec, s[22:23]
	s_cbranch_execz .LBB0_687
	s_lshl_b32 s22, s16, 6
	s_ashr_i32 s23, s22, 31
	s_lshl_b64 s[22:23], s[22:23], 2
	s_add_u32 s22, s17, s22
	s_addc_u32 s23, s20, s23
	s_bcnt1_i32_b64 s14, s[14:15]
	v_mov_b32_e32 v1, 0
	s_waitcnt lgkmcnt(0)
	v_mov_b32_e32 v2, s14
	global_atomic_add v1, v2, s[22:23]
	buffer_inv sc1

;     __device__ __forceinline__ bool run(const f32x4 (&v)[2][2][4][2], const Unit& u, int wr, int wc, int fr, int fq, PG8_LAS unsigned char* lds, int wid, int lane) const {
;     ...
;             bool dead = false; const unsigned long long t0 = __builtin_amdgcn_s_memrealtime();
;             for (;;) {
;                 if ((unsigned)__builtin_amdgcn_readfirstlane(__hip_atomic_load(cnt + 64 * pm, __ATOMIC_RELAXED, __HIP_MEMORY_SCOPE_AGENT)) >= 32u) break;
;                 if (__builtin_amdgcn_s_memrealtime() - t0 > 2000000ull) { if (lane == 0) __hip_atomic_store(tmo, 1u, __ATOMIC_RELAXED, __HIP_MEMORY_SCOPE_AGENT); dead = true; break; }
;                 __builtin_amdgcn_s_sleep(2);
;             }
;             __builtin_amdgcn_fence(__ATOMIC_ACQUIRE, "agent");
;             if (lane == 0) flag[0] = dead ? 1u : 0u;
.LBB0_701:
	s_waitcnt vmcnt(0)
	s_and_b64 exec, exec, s[10:11]
	v_cndmask_b32_e64 v1, 0, 1, s[12:13]
	v_mov_b32_e32 v2, 0
	ds_write_b32 v2, v1 offset:10240

;     __device__ __forceinline__ bool run(const f32x4 (&v)[2][2][4][2], const Unit& u, int wr, int wc, int fr, int fq, PG8_LAS unsigned char* lds, int wid, int lane) const {
;     ...
;         asm volatile("s_waitcnt vmcnt(0)" ::: "memory");
;         if (lane == 0) __hip_atomic_fetch_add(cnt + 64 * pm, 1u, __ATOMIC_RELAXED, __HIP_MEMORY_SCOPE_AGENT);
.LBB0_1001:
	s_or_b64 exec, exec, s[10:11]
	s_waitcnt vmcnt(0)
	s_add_u32 s16, s78, 0x28000
	s_addc_u32 s17, s79, 0
	v_cmp_ne_u32_e64 s[12:13], 0, v203
	v_cmp_eq_u32_e64 s[10:11], 0, v203
	s_and_saveexec_b64 s[4:5], s[10:11]
	s_cbranch_execz .LBB0_1004
	s_mov_b64 s[14:15], exec
	v_mbcnt_lo_u32_b32 v1, s14, 0
	v_mbcnt_hi_u32_b32 v1, s15, v1
	v_cmp_eq_u32_e32 vcc, 0, v1
	s_and_b64 s[24:25], exec, vcc
	s_mov_b64 exec, s[24:25]
	s_cbranch_execz .LBB0_1004
	s_lshl_b32 s24, s3, 6
	s_ashr_i32 s25, s24, 31
	s_lshl_b64 s[24:25], s[24:25], 2
	s_add_u32 s24, s16, s24
	s_addc_u32 s25, s17, s25
	s_bcnt1_i32_b64 s14, s[14:15]
	v_mov_b32_e32 v1, 0
	s_waitcnt lgkmcnt(0)
	v_mov_b32_e32 v2, s14
	global_atomic_add v1, v2, s[24:25]
	buffer_inv sc1
